# scan-phase streaming loads (OI/DST/QD, read once) made non-temporal
# baseline (speedup 1.0000x reference)
; #define LAS __attribute__((address_space(3)))
; template <bool FAKE>
; __device__ __forceinline__ void gla_scan_unit(LAS unsigned char* lds, const bf16_t* qdg, const bf16_t* oig, const bf16_t* dstg, const float* decg, bf16_t* ob, float* ssq,
;                                               int u, int tid, int wave, int lane) {
;     ...
;     f32x4 sst[2]; sst[0] = (f32x4){0.f, 0.f, 0.f, 0.f}; sst[1] = sst[0];
;     { unsigned z0 = 0u; asm volatile("" : "+v"(z0)); *(LAS u32x4*)(STb + tid * 16) = (u32x4){z0, z0, z0, z0}; if (tid < 32) *(LAS u32x4*)(STb + 8192 + tid * 16) = (u32x4){z0, z0, z0, z0}; }
;     const int ub = (b * 4 + h) * 32;
;     struct StepOps { bf16x8 q[4]; u32x2 o; u32x2 ds[2]; f32x4 dc; };
;     const unsigned qoff = (unsigned)((ti * 4 * 64 + fr * 4 + fq) * 16), ooff = (unsigned)(((ti * 2 + tv) * 64 + fr * 4 + fq) * 8);
;     const unsigned dsoff = (unsigned)(((wave * 2) * 64 + fr * 4 + fq) * 8), dcoff = (unsigned)(16 * wave + 4 * fq) * 4u;
;     const char* qbase = (const char*)(qdg + (size_t)(b * 4 + h) * SEQ * 128);
;     const char* obase = (const char*)(oig + ((size_t)(b * 4 + h) * 8 + vs) * SEQ * 32);
;     const char* dsbase = (const char*)(dstg + ((size_t)(b * 4 + h) * 8 + vs) * 32 * 32 * 128);
;     const char* dcbase = (const char*)(decg + (size_t)ub * 128);
;     ...
;     StepOps r0, r1, r2, r3;
;     GLA_LOAD(r0, 0); GLA_LOAD(r1, 1); GLA_LOAD(r2, 2);
;     __syncthreads();
.LBB0_416:
	s_waitcnt vmcnt(8)
	v_mov_b32_e32 v0, v33
	s_nop 0
	v_mov_b32_e32 v1, v0
	v_mov_b32_e32 v2, v0
	v_mov_b32_e32 v3, v0
	ds_write_b128 v168, v[0:3]
	s_and_saveexec_b64 s[2:3], s[4:5]
	ds_write_b128 v168, v[0:3] offset:8192
	s_or_b64 exec, exec, s[2:3]
	s_and_b32 s3, s18, 7
	s_ashr_i32 s10, s19, 5
	s_bfe_u32 s2, s19, 0x20003
	s_lshl_b32 s29, s3, 3
	s_lshl_b32 s31, s3, 6
	s_lshl_b32 s35, s3, 18
	s_lshl_b32 s36, s3, 17
	s_lshl_b32 s3, s10, 2
	s_lshl_b32 s28, s2, 6
	s_lshl_b32 s30, s2, 9
	s_lshl_b32 s34, s2, 5
	s_or_b32 s2, s3, s2
	s_ashr_i32 s3, s2, 31
	s_and_b32 s11, s19, 7
	s_lshl_b32 s20, s2, 5
	s_lshl_b64 s[8:9], s[2:3], 19
	s_add_u32 s22, s12, s8
	s_addc_u32 s23, s13, s9
	s_lshl_b64 s[24:25], s[2:3], 3
	s_or_b32 s24, s24, s11
	s_ashr_i32 s21, s20, 31
	s_lshl_b64 s[26:27], s[24:25], 17
	s_lshl_b64 s[24:25], s[24:25], 18
	s_lshl_b64 s[20:21], s[20:21], 9
	v_lshl_add_u64 v[104:105], s[22:23], 0, v[32:33]
	s_add_u32 s22, s14, s26
	s_movk_i32 s11, 0x4000
	s_addc_u32 s23, s15, s27
	v_add_co_u32_e32 v0, vcc, s11, v104
	s_add_u32 s24, s16, s24
	v_lshl_add_u64 v[106:107], s[22:23], 0, v[82:83]
	v_lshl_add_u64 v[110:111], v[86:87], 0, s[20:21]
	v_addc_co_u32_e32 v1, vcc, 0, v105, vcc
	s_movk_i32 s20, 0x2000
	s_addc_u32 s25, s17, s25
	s_waitcnt vmcnt(0)
	v_add_co_u32_e32 v14, vcc, s20, v106
	v_lshl_add_u64 v[108:109], s[24:25], 0, v[84:85]
	s_nop 0
	v_addc_co_u32_e32 v15, vcc, 0, v107, vcc
	v_add_co_u32_e32 v38, vcc, s20, v108
	s_mov_b64 s[20:21], 0x8000
	s_nop 0
	v_addc_co_u32_e32 v39, vcc, 0, v109, vcc
	v_lshl_add_u64 v[40:41], v[104:105], 0, s[20:21]
	s_mov_b32 s20, 0x8000
	v_add_co_u32_e32 v54, vcc, s20, v104
	s_mov_b64 s[22:23], 0x4000
	s_nop 0
	v_addc_co_u32_e32 v55, vcc, 0, v105, vcc
	v_add_co_u32_e32 v58, vcc, s11, v108
	v_lshl_add_u64 v[12:13], v[104:105], 0, s[22:23]
	v_lshl_add_u64 v[2:3], v[108:109], 0, s[80:81]
	v_lshl_add_u64 v[56:57], v[108:109], 0, s[22:23]
	v_addc_co_u32_e32 v59, vcc, 0, v109, vcc
	global_load_dwordx4 v[24:27], v[104:105], off nt
	global_load_dwordx4 v[20:23], v[104:105], off offset:1024 nt
	global_load_dwordx4 v[16:19], v[104:105], off offset:2048 nt
	global_load_dwordx4 v[8:11], v[104:105], off offset:3072 nt
	global_load_dwordx2 v[144:145], v[106:107], off nt
	global_load_dwordx2 v[114:115], v[108:109], off nt
	global_load_dwordx2 v[112:113], v[108:109], off offset:512 nt
	global_load_dwordx4 v[34:37], v[12:13], off offset:2048 nt
	global_load_dwordx4 v[28:31], v[12:13], off offset:3072 nt
	global_load_dwordx4 v[46:49], v[0:1], off nt
	global_load_dwordx2 v[116:117], v[2:3], off offset:512 nt
	global_load_dwordx4 v[4:7], v[110:111], off nt
	s_nop 0
	global_load_dwordx4 v[0:3], v[110:111], off offset:512 nt
	global_load_dwordx2 v[130:131], v[38:39], off nt
	global_load_dwordx4 v[50:53], v[40:41], off offset:1024 nt
	global_load_dwordx4 v[42:45], v[40:41], off offset:2048 nt
	s_nop 0
	global_load_dwordx4 v[38:41], v[40:41], off offset:3072 nt
	s_nop 0
	global_load_dwordx2 v[146:147], v[14:15], off offset:-4096 nt
	global_load_dwordx2 v[148:149], v[14:15], off nt
	global_load_dwordx2 v[140:141], v[58:59], off nt
	s_nop 0
	global_load_dwordx4 v[58:61], v[54:55], off nt
	global_load_dwordx2 v[132:133], v[56:57], off offset:512 nt
	s_nop 0
	global_load_dwordx4 v[54:57], v[12:13], off offset:1024 nt
	s_nop 0
	global_load_dwordx4 v[12:15], v[110:111], off offset:1024 nt
	s_ashr_i32 s11, s10, 31
	s_lshl_b64 s[22:23], s[10:11], 19
	s_or_b32 s21, s29, s28
	s_or_b32 s22, s22, s21
	v_lshl_add_u64 v[118:119], s[22:23], 0, v[88:89]
	v_lshl_add_u64 v[120:121], s[22:23], 0, v[90:91]
	s_lshl_b64 s[22:23], s[10:11], 22
	s_lshl_b32 s10, s10, 7
	s_or_b32 s11, s31, s30
	s_or_b32 s10, s10, s34
	s_or_b32 s22, s22, s11
	s_ashr_i32 s11, s10, 31
	s_lshl_b64 s[10:11], s[10:11], 9
	v_lshl_add_u64 v[134:135], v[100:101], 0, s[10:11]
	s_lshl_b64 s[10:11], s[2:3], 21
	s_lshl_b64 s[2:3], s[2:3], 20
	s_or_b32 s10, s10, s35
	s_or_b32 s2, s2, s36
	v_mov_b32_e32 v156, 0
	s_mov_b64 s[24:25], 0x4000
	s_mov_b32 s20, 0
	v_lshl_add_u64 v[122:123], s[22:23], 0, v[92:93]
	v_lshl_add_u64 v[124:125], s[22:23], 0, v[94:95]
	v_lshl_add_u64 v[126:127], s[22:23], 0, v[96:97]
	v_lshl_add_u64 v[128:129], s[22:23], 0, v[98:99]
	v_lshl_add_u64 v[136:137], s[10:11], 0, v[84:85]
	v_lshl_add_u64 v[138:139], s[2:3], 0, v[102:103]
	v_lshl_add_u64 v[142:143], v[32:33], 0, s[8:9]
	v_mov_b32_e32 v157, v156
	v_mov_b32_e32 v162, v156
	v_mov_b32_e32 v163, v156
	v_mov_b32_e32 v160, v156
	v_mov_b32_e32 v161, v156
	v_mov_b32_e32 v158, v156
	v_mov_b32_e32 v159, v156
	s_waitcnt lgkmcnt(0)
	s_barrier
	s_branch .LBB0_420

; template <bool FAKE>
; __device__ __forceinline__ void gla_scan_unit(LAS unsigned char* lds, const bf16_t* qdg, const bf16_t* oig, const bf16_t* dstg, const float* decg, bf16_t* ob, float* ssq,
;                                               int u, int tid, int wave, int lane) {
;     ...
;     StepOps r0, r1, r2, r3;
;     GLA_LOAD(r0, 0); GLA_LOAD(r1, 1); GLA_LOAD(r2, 2);
;     __syncthreads();
;     for (int n4 = 0; n4 < 32; n4 += 4) {
;         GLA_LOAD(r3, n4 + 3); GLA_STEP(r0, n4);
;         GLA_LOAD(r0, n4 + 4); GLA_STEP(r1, n4 + 1);
;         GLA_LOAD(r1, n4 + 5); GLA_STEP(r2, n4 + 2);
;         GLA_LOAD(r2, n4 + 6); GLA_STEP(r3, n4 + 3);
.LBB0_420:
	v_lshl_add_u64 v[62:63], s[0:1], 0, v[142:143]
	s_mov_b32 s2, 0x47e0c000
	v_add_co_u32_e32 v66, vcc, s2, v62
	s_waitcnt vmcnt(19)
	v_lshlrev_b32_e32 v150, 16, v144
	v_addc_co_u32_e32 v67, vcc, 0, v63, vcc
	global_load_dwordx4 v[78:81], v[66:67], off nt
	global_load_dwordx4 v[70:73], v[66:67], off offset:1024 nt
	ds_read_b128 v[62:65], v176
	global_load_dwordx4 v[74:77], v[66:67], off offset:2048 nt
	s_nop 0
	global_load_dwordx4 v[66:69], v[66:67], off offset:3072 nt
	ds_read_b128 v[164:167], v176 offset:64
	v_and_b32_e32 v151, 0xffff0000, v144
	v_lshlrev_b32_e32 v152, 16, v145
	v_and_b32_e32 v153, 0xffff0000, v145
	v_lshl_add_u64 v[194:195], s[0:1], 0, v[136:137]
	s_mov_b32 s2, 0x4ae06000
	s_waitcnt lgkmcnt(1)
	v_mfma_f32_16x16x32_bf16 v[24:27], v[62:65], v[24:27], v[150:153]
	ds_read_b128 v[62:65], v176 offset:128
	v_add_co_u32_e32 v144, vcc, s2, v194
	s_waitcnt lgkmcnt(1)
	v_mfma_f32_16x16x32_bf16 v[20:23], v[164:167], v[20:23], v[24:27]
	v_lshl_add_u64 v[154:155], s[0:1], 0, v[138:139]
	v_addc_co_u32_e32 v145, vcc, 0, v195, vcc
	global_load_dwordx2 v[154:155], v[154:155], off nt
	s_nop 0
	global_load_dwordx2 v[152:153], v[144:145], off nt
	global_load_dwordx2 v[150:151], v[144:145], off offset:512 nt
	v_lshl_add_u64 v[144:145], s[0:1], 0, v[134:135]
	s_waitcnt lgkmcnt(0)
	v_mfma_f32_16x16x32_bf16 v[16:19], v[62:65], v[16:19], v[20:23]
	global_load_dwordx4 v[62:65], v[144:145], off nt
	ds_read_b128 v[24:27], v176 offset:192
	s_and_b32 s11, s20, 4
	s_waitcnt lgkmcnt(0)
	v_mfma_f32_16x16x32_bf16 v[8:11], v[24:27], v[8:11], v[16:19]
	s_nop 7
	v_mul_f32_e32 v16, v9, v9
	v_mul_f32_e32 v17, v11, v11
	v_fmac_f32_e32 v16, v8, v8
	v_fmac_f32_e32 v17, v10, v10
	v_add_f32_e32 v17, v16, v17
	ds_swizzle_b32 v18, v17 offset:swizzle(SWAP,16)
	v_cvt_pk_bf16_f32 v16, v8, v9
	s_waitcnt lgkmcnt(0)
	v_add_f32_e32 v8, v17, v18
	ds_bpermute_b32 v9, v170, v8
	v_cvt_pk_bf16_f32 v17, v10, v11
	v_lshl_add_u32 v10, s11, 12, v169
	ds_write_b64 v10, v[16:17] offset:20480
	s_and_saveexec_b64 s[2:3], s[6:7]
	s_cbranch_execz .LBB0_422
	s_waitcnt lgkmcnt(1)
	v_add_f32_e32 v8, v8, v9
	v_lshl_add_u32 v9, s11, 9, v171
	ds_write_b32 v9, v8 offset:53248
.LBB0_422:
	s_or_b64 exec, exec, s[2:3]
	s_waitcnt vmcnt(26)
	v_lshlrev_b32_e32 v8, 16, v114
	s_waitcnt lgkmcnt(1)
	v_and_b32_e32 v9, 0xffff0000, v114
	s_waitcnt vmcnt(20)
	v_pk_fma_f32 v[162:163], v[4:5], v[162:163], v[8:9]
	v_lshlrev_b32_e32 v8, 16, v115
	v_and_b32_e32 v9, 0xffff0000, v115
	v_pk_fma_f32 v[160:161], v[6:7], v[160:161], v[8:9]
	v_cvt_pk_bf16_f32 v8, v162, v163
	v_cvt_pk_bf16_f32 v9, v160, v161
	s_add_i32 s10, s20, 4
	ds_write_b64 v177, v[8:9] offset:8704
	v_lshlrev_b32_e32 v8, 16, v112
	v_and_b32_e32 v9, 0xffff0000, v112
	s_cmp_gt_u32 s20, 27
	v_pk_fma_f32 v[164:165], v[4:5], v[158:159], v[8:9]
	v_lshlrev_b32_e32 v4, 16, v113
	v_and_b32_e32 v5, 0xffff0000, v113
	s_cselect_b64 s[2:3], -1, 0
	s_cmp_lt_u32 s20, 28
	v_pk_fma_f32 v[166:167], v[6:7], v[156:157], v[4:5]
	s_cselect_b32 s96, s10, 31
	v_cvt_pk_bf16_f32 v4, v164, v165
	v_cvt_pk_bf16_f32 v5, v166, v167
	s_lshl_b64 s[8:9], s[96:97], 14
	ds_write_b64 v177, v[4:5] offset:13056
	v_lshl_add_u64 v[4:5], v[104:105], 0, s[8:9]
	s_lshl_b64 s[8:9], s[96:97], 12
	s_waitcnt lgkmcnt(0)
	s_barrier
	global_load_dwordx4 v[24:27], v[4:5], off nt
	global_load_dwordx4 v[20:23], v[4:5], off offset:1024 nt
	global_load_dwordx4 v[16:19], v[4:5], off offset:2048 nt
	global_load_dwordx4 v[8:11], v[4:5], off offset:3072 nt
	v_lshl_add_u64 v[4:5], v[106:107], 0, s[8:9]
	s_lshl_b64 s[8:9], s[96:97], 13
	global_load_dwordx2 v[144:145], v[4:5], off nt
	v_lshl_add_u64 v[4:5], v[108:109], 0, s[8:9]
	s_lshl_b64 s[8:9], s[96:97], 9
	global_load_dwordx2 v[114:115], v[4:5], off nt
	global_load_dwordx2 v[112:113], v[4:5], off offset:512 nt
	v_lshl_add_u64 v[4:5], v[110:111], 0, s[8:9]
	global_load_dwordx4 v[4:7], v[4:5], off nt
	ds_read_b128 v[194:197], v176 offset:8704
	s_waitcnt vmcnt(22)
	v_lshlrev_b32_e32 v156, 16, v146
	v_and_b32_e32 v157, 0xffff0000, v146
	v_lshlrev_b32_e32 v158, 16, v147
	v_and_b32_e32 v159, 0xffff0000, v147
	s_or_b32 s21, s11, 1
	s_waitcnt lgkmcnt(0)
	v_mfma_f32_16x16x32_bf16 v[46:49], v[194:197], v[46:49], v[156:159]
	s_nop 2
	ds_read_b128 v[156:159], v176 offset:8768
	s_waitcnt vmcnt(17) lgkmcnt(0)
	v_mfma_f32_16x16x32_bf16 v[46:49], v[156:159], v[54:57], v[46:49]
	ds_read_b128 v[54:57], v176 offset:8832
	s_waitcnt lgkmcnt(0)
	v_mfma_f32_16x16x32_bf16 v[34:37], v[54:57], v[34:37], v[46:49]
	s_nop 4
	ds_read_b128 v[46:49], v176 offset:8896
	s_waitcnt lgkmcnt(0)
	v_mfma_f32_16x16x32_bf16 v[28:31], v[46:49], v[28:31], v[34:37]
	s_nop 2
	v_lshl_add_u32 v36, s21, 12, v169
	s_nop 3
	v_cvt_pk_bf16_f32 v34, v28, v29
	v_mul_f32_e32 v29, v29, v29
	v_fmac_f32_e32 v29, v28, v28
	v_mul_f32_e32 v28, v31, v31
	v_fmac_f32_e32 v28, v30, v30
	v_add_f32_e32 v28, v29, v28
	ds_swizzle_b32 v29, v28 offset:swizzle(SWAP,16)
	v_cvt_pk_bf16_f32 v35, v30, v31
	ds_write_b64 v36, v[34:35] offset:20480
	s_waitcnt lgkmcnt(1)
	v_add_f32_e32 v28, v28, v29
	ds_bpermute_b32 v29, v170, v28
	s_and_saveexec_b64 s[8:9], s[6:7]
	s_cbranch_execz .LBB0_424
	s_waitcnt lgkmcnt(0)
	v_add_f32_e32 v28, v28, v29
	v_lshl_add_u32 v29, s21, 9, v171
	ds_write_b32 v29, v28 offset:53248
; template <bool FAKE>
; __device__ __forceinline__ void gla_scan_unit(LAS unsigned char* lds, const bf16_t* qdg, const bf16_t* oig, const bf16_t* dstg, const float* decg, bf16_t* ob, float* ssq,
;                                               int u, int tid, int wave, int lane) {
;     ...
;     StepOps r0, r1, r2, r3;
;     GLA_LOAD(r0, 0); GLA_LOAD(r1, 1); GLA_LOAD(r2, 2);
;     __syncthreads();
;     for (int n4 = 0; n4 < 32; n4 += 4) {
;         GLA_LOAD(r3, n4 + 3); GLA_STEP(r0, n4);
;         GLA_LOAD(r0, n4 + 4); GLA_STEP(r1, n4 + 1);
;         GLA_LOAD(r1, n4 + 5); GLA_STEP(r2, n4 + 2);
;         GLA_LOAD(r2, n4 + 6); GLA_STEP(r3, n4 + 3);
.LBB0_424:
	s_or_b64 exec, exec, s[8:9]
	v_lshlrev_b32_e32 v28, 16, v130
	s_waitcnt lgkmcnt(0)
	v_and_b32_e32 v29, 0xffff0000, v130
	v_pk_fma_f32 v[156:157], v[0:1], v[162:163], v[28:29]
	v_lshlrev_b32_e32 v28, 16, v131
	v_and_b32_e32 v29, 0xffff0000, v131
	v_pk_fma_f32 v[158:159], v[2:3], v[160:161], v[28:29]
	v_cvt_pk_bf16_f32 v28, v156, v157
	v_cvt_pk_bf16_f32 v29, v158, v159
	ds_write_b64 v177, v[28:29]
	v_lshlrev_b32_e32 v28, 16, v116
	v_and_b32_e32 v29, 0xffff0000, v116
	v_pk_fma_f32 v[160:161], v[0:1], v[164:165], v[28:29]
	v_lshlrev_b32_e32 v0, 16, v117
	v_and_b32_e32 v1, 0xffff0000, v117
	s_min_u32 s8, s20, 26
	v_pk_fma_f32 v[162:163], v[2:3], v[166:167], v[0:1]
	s_add_i32 s8, s8, 5
	v_cvt_pk_bf16_f32 v0, v160, v161
	v_cvt_pk_bf16_f32 v1, v162, v163
	s_lshl_b32 s96, s8, 14
	ds_write_b64 v177, v[0:1] offset:4352
	v_lshl_add_u64 v[0:1], v[104:105], 0, s[96:97]
	s_lshl_b32 s96, s8, 12
	s_waitcnt lgkmcnt(0)
	s_barrier
	global_load_dwordx4 v[46:49], v[0:1], off nt
	global_load_dwordx4 v[54:57], v[0:1], off offset:1024 nt
	global_load_dwordx4 v[34:37], v[0:1], off offset:2048 nt
	global_load_dwordx4 v[28:31], v[0:1], off offset:3072 nt
	v_lshl_add_u64 v[0:1], v[106:107], 0, s[96:97]
	s_lshl_b32 s96, s8, 13
	global_load_dwordx2 v[146:147], v[0:1], off nt
	v_lshl_add_u64 v[0:1], v[108:109], 0, s[96:97]
	s_lshl_b32 s96, s8, 9
	global_load_dwordx2 v[130:131], v[0:1], off nt
	global_load_dwordx2 v[116:117], v[0:1], off offset:512 nt
	v_lshl_add_u64 v[0:1], v[110:111], 0, s[96:97]
	global_load_dwordx4 v[0:3], v[0:1], off nt
	ds_read_b128 v[194:197], v176
	v_lshlrev_b32_e32 v164, 16, v148
	v_and_b32_e32 v165, 0xffff0000, v148
	v_lshlrev_b32_e32 v166, 16, v149
	v_and_b32_e32 v167, 0xffff0000, v149
	s_or_b32 s11, s11, 2
	s_waitcnt lgkmcnt(0)
	v_mfma_f32_16x16x32_bf16 v[58:61], v[194:197], v[58:61], v[164:167]
	s_nop 2
	ds_read_b128 v[164:167], v176 offset:64
	s_waitcnt lgkmcnt(0)
	v_mfma_f32_16x16x32_bf16 v[50:53], v[164:167], v[50:53], v[58:61]
	s_nop 2
	ds_read_b128 v[58:61], v176 offset:128
	s_waitcnt lgkmcnt(0)
	v_mfma_f32_16x16x32_bf16 v[42:45], v[58:61], v[42:45], v[50:53]
	s_nop 2
	ds_read_b128 v[50:53], v176 offset:192
	s_waitcnt lgkmcnt(0)
	v_mfma_f32_16x16x32_bf16 v[38:41], v[50:53], v[38:41], v[42:45]
	s_nop 2
	v_lshl_add_u32 v44, s11, 12, v169
	s_nop 3
	v_cvt_pk_bf16_f32 v42, v38, v39
	v_mul_f32_e32 v39, v39, v39
	v_fmac_f32_e32 v39, v38, v38
	v_mul_f32_e32 v38, v41, v41
	v_fmac_f32_e32 v38, v40, v40
	v_add_f32_e32 v38, v39, v38
	ds_swizzle_b32 v39, v38 offset:swizzle(SWAP,16)
	v_cvt_pk_bf16_f32 v43, v40, v41
	ds_write_b64 v44, v[42:43] offset:20480
	s_waitcnt lgkmcnt(1)
	v_add_f32_e32 v38, v38, v39
	ds_bpermute_b32 v39, v170, v38
	s_and_saveexec_b64 s[8:9], s[6:7]
	s_cbranch_execz .LBB0_426
	s_waitcnt lgkmcnt(0)
	v_add_f32_e32 v38, v38, v39
	v_lshl_add_u32 v39, s11, 9, v171
	ds_write_b32 v39, v38 offset:53248
.LBB0_426:
	s_or_b64 exec, exec, s[8:9]
	v_lshlrev_b32_e32 v38, 16, v140
	s_waitcnt lgkmcnt(0)
	v_and_b32_e32 v39, 0xffff0000, v140
	s_waitcnt vmcnt(24)
	v_pk_fma_f32 v[156:157], v[12:13], v[156:157], v[38:39]
	v_lshlrev_b32_e32 v38, 16, v141
	v_and_b32_e32 v39, 0xffff0000, v141
	v_pk_fma_f32 v[158:159], v[14:15], v[158:159], v[38:39]
	v_cvt_pk_bf16_f32 v38, v156, v157
	v_cvt_pk_bf16_f32 v39, v158, v159
	ds_write_b64 v177, v[38:39] offset:8704
	v_lshlrev_b32_e32 v38, 16, v132
	v_and_b32_e32 v39, 0xffff0000, v132
	v_pk_fma_f32 v[164:165], v[12:13], v[160:161], v[38:39]
	v_lshlrev_b32_e32 v12, 16, v133
	v_and_b32_e32 v13, 0xffff0000, v133
	s_min_u32 s9, s20, 25
	v_pk_fma_f32 v[166:167], v[14:15], v[162:163], v[12:13]
	s_add_i32 s9, s9, 6
	v_cvt_pk_bf16_f32 v12, v164, v165
	v_cvt_pk_bf16_f32 v13, v166, v167
	s_lshl_b32 s96, s9, 14
	ds_write_b64 v177, v[12:13] offset:13056
	v_lshl_add_u64 v[12:13], v[104:105], 0, s[96:97]
	s_lshl_b32 s96, s9, 12
	s_waitcnt lgkmcnt(0)
	s_barrier
	global_load_dwordx4 v[58:61], v[12:13], off nt
	global_load_dwordx4 v[50:53], v[12:13], off offset:1024 nt
	global_load_dwordx4 v[42:45], v[12:13], off offset:2048 nt
	global_load_dwordx4 v[38:41], v[12:13], off offset:3072 nt
	v_lshl_add_u64 v[12:13], v[106:107], 0, s[96:97]
	s_lshl_b32 s96, s9, 13
	global_load_dwordx2 v[148:149], v[12:13], off nt
	v_lshl_add_u64 v[12:13], v[108:109], 0, s[96:97]
	s_lshl_b32 s96, s9, 9
	global_load_dwordx2 v[140:141], v[12:13], off nt
	global_load_dwordx2 v[132:133], v[12:13], off offset:512 nt
	v_lshl_add_u64 v[12:13], v[110:111], 0, s[96:97]
	global_load_dwordx4 v[12:15], v[12:13], off nt
	ds_read_b128 v[194:197], v176 offset:8704
	s_waitcnt vmcnt(27)
	v_lshlrev_b32_e32 v160, 16, v154
	v_and_b32_e32 v161, 0xffff0000, v154
	v_lshlrev_b32_e32 v162, 16, v155
	v_and_b32_e32 v163, 0xffff0000, v155
	s_add_i32 s8, s20, 3
	s_and_b32 s11, s8, 7
	s_waitcnt lgkmcnt(0)
	v_mfma_f32_16x16x32_bf16 v[78:81], v[194:197], v[78:81], v[160:163]
	s_nop 2
	ds_read_b128 v[160:163], v176 offset:8768
	s_waitcnt lgkmcnt(0)
	v_mfma_f32_16x16x32_bf16 v[70:73], v[160:163], v[70:73], v[78:81]
	s_nop 2
	ds_read_b128 v[78:81], v176 offset:8832
	s_waitcnt lgkmcnt(0)
	v_mfma_f32_16x16x32_bf16 v[70:73], v[78:81], v[74:77], v[70:73]
	ds_read_b128 v[74:77], v176 offset:8896
	s_waitcnt lgkmcnt(0)
	v_mfma_f32_16x16x32_bf16 v[66:69], v[74:77], v[66:69], v[70:73]
	s_nop 4
	v_lshl_add_u32 v72, s11, 12, v169
	s_nop 1
	v_cvt_pk_bf16_f32 v70, v66, v67
	v_mul_f32_e32 v67, v67, v67
	v_fmac_f32_e32 v67, v66, v66
	v_mul_f32_e32 v66, v69, v69
	v_fmac_f32_e32 v66, v68, v68
	v_add_f32_e32 v66, v67, v66
	ds_swizzle_b32 v67, v66 offset:swizzle(SWAP,16)
	v_cvt_pk_bf16_f32 v71, v68, v69
	ds_write_b64 v72, v[70:71] offset:20480
	s_waitcnt lgkmcnt(1)
	v_add_f32_e32 v66, v66, v67
	ds_bpermute_b32 v67, v170, v66
	s_and_saveexec_b64 s[8:9], s[6:7]
	s_cbranch_execz .LBB0_428
	s_waitcnt lgkmcnt(0)
	v_add_f32_e32 v66, v66, v67
	v_lshl_add_u32 v67, s11, 9, v171
	ds_write_b32 v67, v66 offset:53248
